# v93 + phase E mid-K merge-gate hook: counted vmcnt ladder (14..0) over the 16 gate loads so unpack/rcp/scale of early vectors overlaps arrival of later ones
# speedup vs baseline: 1.0127x; 1.0093x over previous
.LBB0_3865:
	v_mov_b32_e32 v130, v246
	s_cmpk_eq_i32 s20, 0x400
	v_add_u32_e32 v130, s50, v130
	s_cselect_b32 s0, 0, 0x800
	v_mul_lo_u32 v130, v130, s64
	v_or_b32_e32 v131, s17, v249
	v_add3_u32 v130, v131, s0, v130
	v_add_u32_e32 v131, 0x18000, v130
	global_load_dwordx4 v[186:189], v130, s[10:11]
	global_load_dwordx4 v[190:193], v130, s[10:11] offset:2048
	global_load_dwordx4 v[178:181], v131, s[10:11]
	global_load_dwordx4 v[182:185], v131, s[10:11] offset:2048
	v_add_u32_e32 v131, 0x30000, v130
	global_load_dwordx4 v[170:173], v131, s[10:11]
	global_load_dwordx4 v[174:177], v131, s[10:11] offset:2048
	v_add_u32_e32 v131, 0x48000, v130
	global_load_dwordx4 v[162:165], v131, s[10:11]
	global_load_dwordx4 v[166:169], v131, s[10:11] offset:2048
	v_add_u32_e32 v131, 0xc0000, v130
	global_load_dwordx4 v[154:157], v131, s[10:11]
	global_load_dwordx4 v[158:161], v131, s[10:11] offset:2048
	v_add_u32_e32 v131, 0xd8000, v130
	global_load_dwordx4 v[146:149], v131, s[10:11]
	global_load_dwordx4 v[150:153], v131, s[10:11] offset:2048
	v_add_u32_e32 v131, 0xf0000, v130
	v_add_u32_e32 v134, 0x108000, v130
	global_load_dwordx4 v[138:141], v131, s[10:11]
	global_load_dwordx4 v[142:145], v131, s[10:11] offset:2048
	s_nop 0
	global_load_dwordx4 v[130:133], v134, s[10:11]
	s_nop 0
	global_load_dwordx4 v[134:137], v134, s[10:11] offset:2048
	s_nop 0
	s_nop 0
	s_waitcnt vmcnt(14)
	v_cvt_f32_ubyte0_e32 v203, v190
	v_cvt_f32_ubyte1_e32 v205, v190
	v_cvt_f32_ubyte2_e32 v207, v190
	v_cvt_f32_ubyte3_e32 v213, v190
	v_cvt_f32_ubyte0_e32 v214, v191
	v_cvt_f32_ubyte1_e32 v215, v191
	v_cvt_f32_ubyte2_e32 v223, v191
	v_cvt_f32_ubyte3_e32 v225, v191
	v_rcp_iflag_f32_e32 v190, v203
	v_rcp_iflag_f32_e32 v191, v205
	v_rcp_iflag_f32_e32 v212, v207
	v_rcp_iflag_f32_e32 v213, v213
	v_rcp_iflag_f32_e32 v214, v214
	v_rcp_iflag_f32_e32 v215, v215
	v_rcp_iflag_f32_e32 v224, v223
	v_rcp_iflag_f32_e32 v225, v225
	v_cvt_f32_ubyte3_e32 v227, v186
	v_cvt_f32_ubyte2_e32 v226, v186
	v_cvt_f32_ubyte1_e32 v231, v186
	v_cvt_f32_ubyte0_e32 v230, v186
	v_pk_mul_f32 v[190:191], v[190:191], v[230:231]
	v_pk_mul_f32 v[212:213], v[212:213], v[226:227]
	v_pk_mul_f32 v[126:127], v[126:127], v[190:191]
	v_pk_mul_f32 v[128:129], v[128:129], v[212:213]
	v_cvt_f32_ubyte3_e32 v191, v187
	v_cvt_f32_ubyte2_e32 v190, v187
	v_cvt_f32_ubyte1_e32 v213, v187
	v_cvt_f32_ubyte0_e32 v212, v187
	v_pk_mul_f32 v[186:187], v[214:215], v[212:213]
	v_pk_mul_f32 v[190:191], v[224:225], v[190:191]
	v_pk_mul_f32 v[122:123], v[122:123], v[186:187]
	v_pk_mul_f32 v[124:125], v[124:125], v[190:191]
	v_cvt_f32_ubyte0_e32 v186, v192
	v_cvt_f32_ubyte1_e32 v187, v192
	v_cvt_f32_ubyte2_e32 v190, v192
	v_cvt_f32_ubyte3_e32 v191, v192
	v_rcp_iflag_f32_e32 v186, v186
	v_rcp_iflag_f32_e32 v187, v187
	v_rcp_iflag_f32_e32 v190, v190
	v_rcp_iflag_f32_e32 v191, v191
	v_cvt_f32_ubyte0_e32 v192, v193
	v_cvt_f32_ubyte1_e32 v203, v193
	v_cvt_f32_ubyte2_e32 v205, v193
	v_cvt_f32_ubyte3_e32 v207, v193
	v_rcp_iflag_f32_e32 v192, v192
	v_rcp_iflag_f32_e32 v193, v203
	v_rcp_iflag_f32_e32 v212, v205
	v_rcp_iflag_f32_e32 v213, v207
	v_cvt_f32_ubyte3_e32 v215, v188
	v_cvt_f32_ubyte2_e32 v214, v188
	v_cvt_f32_ubyte1_e32 v225, v188
	v_cvt_f32_ubyte0_e32 v224, v188
	v_pk_mul_f32 v[186:187], v[186:187], v[224:225]
	v_pk_mul_f32 v[190:191], v[190:191], v[214:215]
	v_pk_mul_f32 v[118:119], v[118:119], v[186:187]
	v_pk_mul_f32 v[120:121], v[120:121], v[190:191]
	v_cvt_f32_ubyte3_e32 v187, v189
	v_cvt_f32_ubyte2_e32 v186, v189
	v_cvt_f32_ubyte1_e32 v191, v189
	v_cvt_f32_ubyte0_e32 v190, v189
	v_pk_mul_f32 v[188:189], v[192:193], v[190:191]
	v_pk_mul_f32 v[186:187], v[212:213], v[186:187]
	v_pk_mul_f32 v[114:115], v[114:115], v[188:189]
	v_pk_mul_f32 v[116:117], v[116:117], v[186:187]
	s_waitcnt vmcnt(12)
	v_cvt_f32_ubyte0_e32 v186, v182
	v_cvt_f32_ubyte1_e32 v187, v182
	v_cvt_f32_ubyte2_e32 v188, v182
	v_cvt_f32_ubyte3_e32 v189, v182
	v_cvt_f32_ubyte0_e32 v190, v183
	v_cvt_f32_ubyte1_e32 v191, v183
	v_cvt_f32_ubyte2_e32 v192, v183
	v_cvt_f32_ubyte3_e32 v193, v183
	v_rcp_iflag_f32_e32 v182, v186
	v_rcp_iflag_f32_e32 v183, v187
	v_rcp_iflag_f32_e32 v186, v188
	v_rcp_iflag_f32_e32 v187, v189
	v_rcp_iflag_f32_e32 v188, v190
	v_rcp_iflag_f32_e32 v189, v191
	v_rcp_iflag_f32_e32 v190, v192
	v_rcp_iflag_f32_e32 v191, v193
	v_cvt_f32_ubyte3_e32 v193, v178
	v_cvt_f32_ubyte2_e32 v192, v178
	v_cvt_f32_ubyte1_e32 v213, v178
	v_cvt_f32_ubyte0_e32 v212, v178
	v_pk_mul_f32 v[182:183], v[182:183], v[212:213]
	v_pk_mul_f32 v[186:187], v[186:187], v[192:193]
	v_pk_mul_f32 v[110:111], v[110:111], v[182:183]
	v_pk_mul_f32 v[112:113], v[112:113], v[186:187]
	v_cvt_f32_ubyte3_e32 v183, v179
	v_cvt_f32_ubyte2_e32 v182, v179
	v_cvt_f32_ubyte1_e32 v187, v179
	v_cvt_f32_ubyte0_e32 v186, v179
	v_pk_mul_f32 v[178:179], v[188:189], v[186:187]
	v_pk_mul_f32 v[182:183], v[190:191], v[182:183]
	v_pk_mul_f32 v[106:107], v[106:107], v[178:179]
	v_pk_mul_f32 v[108:109], v[108:109], v[182:183]
	v_cvt_f32_ubyte0_e32 v178, v184
	v_cvt_f32_ubyte1_e32 v179, v184
	v_cvt_f32_ubyte2_e32 v182, v184
	v_cvt_f32_ubyte3_e32 v183, v184
	v_rcp_iflag_f32_e32 v178, v178
	v_rcp_iflag_f32_e32 v179, v179
	v_rcp_iflag_f32_e32 v182, v182
	v_rcp_iflag_f32_e32 v183, v183
	v_cvt_f32_ubyte0_e32 v184, v185
	v_cvt_f32_ubyte1_e32 v186, v185
	v_cvt_f32_ubyte2_e32 v187, v185
	v_cvt_f32_ubyte3_e32 v188, v185
	v_rcp_iflag_f32_e32 v184, v184
	v_rcp_iflag_f32_e32 v185, v186
	v_rcp_iflag_f32_e32 v186, v187
	v_rcp_iflag_f32_e32 v187, v188
	v_cvt_f32_ubyte3_e32 v189, v180
	v_cvt_f32_ubyte2_e32 v188, v180
	v_cvt_f32_ubyte1_e32 v191, v180
	v_cvt_f32_ubyte0_e32 v190, v180
	v_pk_mul_f32 v[178:179], v[178:179], v[190:191]
	v_pk_mul_f32 v[182:183], v[182:183], v[188:189]
	v_pk_mul_f32 v[102:103], v[102:103], v[178:179]
	v_pk_mul_f32 v[104:105], v[104:105], v[182:183]
	v_cvt_f32_ubyte3_e32 v179, v181
	v_cvt_f32_ubyte2_e32 v178, v181
	v_cvt_f32_ubyte1_e32 v183, v181
	v_cvt_f32_ubyte0_e32 v182, v181
	v_pk_mul_f32 v[180:181], v[184:185], v[182:183]
	v_pk_mul_f32 v[178:179], v[186:187], v[178:179]
	v_pk_mul_f32 v[98:99], v[98:99], v[180:181]
	v_pk_mul_f32 v[100:101], v[100:101], v[178:179]
	s_waitcnt vmcnt(10)
	v_cvt_f32_ubyte0_e32 v178, v174
	v_cvt_f32_ubyte1_e32 v179, v174
	v_cvt_f32_ubyte2_e32 v180, v174
	v_cvt_f32_ubyte3_e32 v181, v174
	v_cvt_f32_ubyte0_e32 v182, v175
	v_cvt_f32_ubyte1_e32 v183, v175
	v_cvt_f32_ubyte2_e32 v184, v175
	v_cvt_f32_ubyte3_e32 v185, v175
	v_rcp_iflag_f32_e32 v174, v178
	v_rcp_iflag_f32_e32 v175, v179
	v_rcp_iflag_f32_e32 v178, v180
	v_rcp_iflag_f32_e32 v179, v181
	v_rcp_iflag_f32_e32 v180, v182
	v_rcp_iflag_f32_e32 v181, v183
	v_rcp_iflag_f32_e32 v182, v184
	v_rcp_iflag_f32_e32 v183, v185
	v_cvt_f32_ubyte3_e32 v185, v170
	v_cvt_f32_ubyte2_e32 v184, v170
	v_cvt_f32_ubyte1_e32 v187, v170
	v_cvt_f32_ubyte0_e32 v186, v170
	v_pk_mul_f32 v[174:175], v[174:175], v[186:187]
	v_pk_mul_f32 v[178:179], v[178:179], v[184:185]
	v_pk_mul_f32 v[94:95], v[94:95], v[174:175]
	v_pk_mul_f32 v[96:97], v[96:97], v[178:179]
	v_cvt_f32_ubyte3_e32 v175, v171
	v_cvt_f32_ubyte2_e32 v174, v171
	v_cvt_f32_ubyte1_e32 v179, v171
	v_cvt_f32_ubyte0_e32 v178, v171
	v_pk_mul_f32 v[170:171], v[180:181], v[178:179]
	v_pk_mul_f32 v[174:175], v[182:183], v[174:175]
	v_pk_mul_f32 v[90:91], v[90:91], v[170:171]
	v_pk_mul_f32 v[92:93], v[92:93], v[174:175]
	v_cvt_f32_ubyte0_e32 v170, v176
	v_cvt_f32_ubyte1_e32 v171, v176
	v_cvt_f32_ubyte2_e32 v174, v176
	v_cvt_f32_ubyte3_e32 v175, v176
	v_rcp_iflag_f32_e32 v170, v170
	v_rcp_iflag_f32_e32 v171, v171
	v_rcp_iflag_f32_e32 v174, v174
	v_rcp_iflag_f32_e32 v175, v175
	v_cvt_f32_ubyte0_e32 v176, v177
	v_cvt_f32_ubyte1_e32 v178, v177
	v_cvt_f32_ubyte2_e32 v179, v177
	v_cvt_f32_ubyte3_e32 v180, v177
	v_rcp_iflag_f32_e32 v176, v176
	v_rcp_iflag_f32_e32 v177, v178
	v_rcp_iflag_f32_e32 v178, v179
	v_rcp_iflag_f32_e32 v179, v180
	v_cvt_f32_ubyte3_e32 v181, v172
	v_cvt_f32_ubyte2_e32 v180, v172
	v_cvt_f32_ubyte1_e32 v183, v172
	v_cvt_f32_ubyte0_e32 v182, v172
	v_pk_mul_f32 v[170:171], v[170:171], v[182:183]
	v_pk_mul_f32 v[174:175], v[174:175], v[180:181]
	v_pk_mul_f32 v[86:87], v[86:87], v[170:171]
	v_pk_mul_f32 v[88:89], v[88:89], v[174:175]
	v_cvt_f32_ubyte3_e32 v171, v173
	v_cvt_f32_ubyte2_e32 v170, v173
	v_cvt_f32_ubyte1_e32 v175, v173
	v_cvt_f32_ubyte0_e32 v174, v173
	v_pk_mul_f32 v[172:173], v[176:177], v[174:175]
	v_pk_mul_f32 v[170:171], v[178:179], v[170:171]
	v_pk_mul_f32 v[82:83], v[82:83], v[172:173]
	v_pk_mul_f32 v[84:85], v[84:85], v[170:171]
	s_waitcnt vmcnt(8)
	v_cvt_f32_ubyte0_e32 v170, v166
	v_cvt_f32_ubyte1_e32 v171, v166
	v_cvt_f32_ubyte2_e32 v172, v166
	v_cvt_f32_ubyte3_e32 v173, v166
	v_cvt_f32_ubyte0_e32 v174, v167
	v_cvt_f32_ubyte1_e32 v175, v167
	v_cvt_f32_ubyte2_e32 v176, v167
	v_cvt_f32_ubyte3_e32 v177, v167
	v_rcp_iflag_f32_e32 v166, v170
	v_rcp_iflag_f32_e32 v167, v171
	v_rcp_iflag_f32_e32 v170, v172
	v_rcp_iflag_f32_e32 v171, v173
	v_rcp_iflag_f32_e32 v172, v174
	v_rcp_iflag_f32_e32 v173, v175
	v_rcp_iflag_f32_e32 v174, v176
	v_rcp_iflag_f32_e32 v175, v177
	v_cvt_f32_ubyte3_e32 v177, v162
	v_cvt_f32_ubyte2_e32 v176, v162
	v_cvt_f32_ubyte1_e32 v179, v162
	v_cvt_f32_ubyte0_e32 v178, v162
	v_pk_mul_f32 v[166:167], v[166:167], v[178:179]
	v_pk_mul_f32 v[170:171], v[170:171], v[176:177]
	v_pk_mul_f32 v[78:79], v[78:79], v[166:167]
	v_pk_mul_f32 v[80:81], v[80:81], v[170:171]
	v_cvt_f32_ubyte3_e32 v167, v163
	v_cvt_f32_ubyte2_e32 v166, v163
	v_cvt_f32_ubyte1_e32 v171, v163
	v_cvt_f32_ubyte0_e32 v170, v163
	v_pk_mul_f32 v[162:163], v[172:173], v[170:171]
	v_pk_mul_f32 v[166:167], v[174:175], v[166:167]
	v_pk_mul_f32 v[74:75], v[74:75], v[162:163]
	v_pk_mul_f32 v[76:77], v[76:77], v[166:167]
	v_cvt_f32_ubyte0_e32 v162, v168
	v_cvt_f32_ubyte1_e32 v163, v168
	v_cvt_f32_ubyte2_e32 v166, v168
	v_cvt_f32_ubyte3_e32 v167, v168
	v_rcp_iflag_f32_e32 v162, v162
	v_rcp_iflag_f32_e32 v163, v163
	v_rcp_iflag_f32_e32 v166, v166
	v_rcp_iflag_f32_e32 v167, v167
	v_cvt_f32_ubyte0_e32 v168, v169
	v_cvt_f32_ubyte1_e32 v170, v169
	v_cvt_f32_ubyte2_e32 v171, v169
	v_cvt_f32_ubyte3_e32 v172, v169
	v_rcp_iflag_f32_e32 v168, v168
	v_rcp_iflag_f32_e32 v169, v170
	v_rcp_iflag_f32_e32 v170, v171
	v_rcp_iflag_f32_e32 v171, v172
	v_cvt_f32_ubyte3_e32 v173, v164
	v_cvt_f32_ubyte2_e32 v172, v164
	v_cvt_f32_ubyte1_e32 v175, v164
	v_cvt_f32_ubyte0_e32 v174, v164
	v_pk_mul_f32 v[162:163], v[162:163], v[174:175]
	v_pk_mul_f32 v[166:167], v[166:167], v[172:173]
	v_pk_mul_f32 v[70:71], v[70:71], v[162:163]
	v_pk_mul_f32 v[72:73], v[72:73], v[166:167]
	v_cvt_f32_ubyte3_e32 v163, v165
	v_cvt_f32_ubyte2_e32 v162, v165
	v_cvt_f32_ubyte1_e32 v167, v165
	v_cvt_f32_ubyte0_e32 v166, v165
	v_pk_mul_f32 v[164:165], v[168:169], v[166:167]
	v_pk_mul_f32 v[162:163], v[170:171], v[162:163]
	v_pk_mul_f32 v[66:67], v[66:67], v[164:165]
	v_pk_mul_f32 v[68:69], v[68:69], v[162:163]
	s_waitcnt vmcnt(6)
	v_cvt_f32_ubyte0_e32 v162, v158
	v_cvt_f32_ubyte1_e32 v163, v158
	v_cvt_f32_ubyte2_e32 v164, v158
	v_cvt_f32_ubyte3_e32 v165, v158
	v_cvt_f32_ubyte0_e32 v166, v159
	v_cvt_f32_ubyte1_e32 v167, v159
	v_cvt_f32_ubyte2_e32 v168, v159
	v_cvt_f32_ubyte3_e32 v169, v159
	v_rcp_iflag_f32_e32 v158, v162
	v_rcp_iflag_f32_e32 v159, v163
	v_rcp_iflag_f32_e32 v162, v164
	v_rcp_iflag_f32_e32 v163, v165
	v_rcp_iflag_f32_e32 v164, v166
	v_rcp_iflag_f32_e32 v165, v167
	v_rcp_iflag_f32_e32 v166, v168
	v_rcp_iflag_f32_e32 v167, v169
	v_cvt_f32_ubyte3_e32 v169, v154
	v_cvt_f32_ubyte2_e32 v168, v154
	v_cvt_f32_ubyte1_e32 v171, v154
	v_cvt_f32_ubyte0_e32 v170, v154
	v_pk_mul_f32 v[158:159], v[158:159], v[170:171]
	v_pk_mul_f32 v[162:163], v[162:163], v[168:169]
	v_pk_mul_f32 v[62:63], v[62:63], v[158:159]
	v_pk_mul_f32 v[64:65], v[64:65], v[162:163]
	v_cvt_f32_ubyte3_e32 v159, v155
	v_cvt_f32_ubyte2_e32 v158, v155
	v_cvt_f32_ubyte1_e32 v163, v155
	v_cvt_f32_ubyte0_e32 v162, v155
	v_pk_mul_f32 v[154:155], v[164:165], v[162:163]
	v_pk_mul_f32 v[158:159], v[166:167], v[158:159]
	v_pk_mul_f32 v[58:59], v[58:59], v[154:155]
	v_pk_mul_f32 v[60:61], v[60:61], v[158:159]
	v_cvt_f32_ubyte0_e32 v154, v160
	v_cvt_f32_ubyte1_e32 v155, v160
	v_cvt_f32_ubyte2_e32 v158, v160
	v_cvt_f32_ubyte3_e32 v159, v160
	v_rcp_iflag_f32_e32 v154, v154
	v_rcp_iflag_f32_e32 v155, v155
	v_rcp_iflag_f32_e32 v158, v158
	v_rcp_iflag_f32_e32 v159, v159
	v_cvt_f32_ubyte0_e32 v160, v161
	v_cvt_f32_ubyte1_e32 v162, v161
	v_cvt_f32_ubyte2_e32 v163, v161
	v_cvt_f32_ubyte3_e32 v164, v161
	v_rcp_iflag_f32_e32 v160, v160
	v_rcp_iflag_f32_e32 v161, v162
	v_rcp_iflag_f32_e32 v162, v163
	v_rcp_iflag_f32_e32 v163, v164
	v_cvt_f32_ubyte3_e32 v165, v156
	v_cvt_f32_ubyte2_e32 v164, v156
	v_cvt_f32_ubyte1_e32 v167, v156
	v_cvt_f32_ubyte0_e32 v166, v156
	v_pk_mul_f32 v[154:155], v[154:155], v[166:167]
	v_pk_mul_f32 v[158:159], v[158:159], v[164:165]
	v_pk_mul_f32 v[54:55], v[54:55], v[154:155]
	v_pk_mul_f32 v[56:57], v[56:57], v[158:159]
	v_cvt_f32_ubyte3_e32 v155, v157
	v_cvt_f32_ubyte2_e32 v154, v157
	v_cvt_f32_ubyte1_e32 v159, v157
	v_cvt_f32_ubyte0_e32 v158, v157
	v_pk_mul_f32 v[156:157], v[160:161], v[158:159]
	v_pk_mul_f32 v[154:155], v[162:163], v[154:155]
	v_pk_mul_f32 v[50:51], v[50:51], v[156:157]
	v_pk_mul_f32 v[52:53], v[52:53], v[154:155]
	s_waitcnt vmcnt(4)
	v_cvt_f32_ubyte0_e32 v154, v150
	v_cvt_f32_ubyte1_e32 v155, v150
	v_cvt_f32_ubyte2_e32 v156, v150
	v_cvt_f32_ubyte3_e32 v157, v150
	v_cvt_f32_ubyte0_e32 v158, v151
	v_cvt_f32_ubyte1_e32 v159, v151
	v_cvt_f32_ubyte2_e32 v160, v151
	v_cvt_f32_ubyte3_e32 v161, v151
	v_rcp_iflag_f32_e32 v150, v154
	v_rcp_iflag_f32_e32 v151, v155
	v_rcp_iflag_f32_e32 v154, v156
	v_rcp_iflag_f32_e32 v155, v157
	v_rcp_iflag_f32_e32 v156, v158
	v_rcp_iflag_f32_e32 v157, v159
	v_rcp_iflag_f32_e32 v158, v160
	v_rcp_iflag_f32_e32 v159, v161
	v_cvt_f32_ubyte3_e32 v161, v146
	v_cvt_f32_ubyte2_e32 v160, v146
	v_cvt_f32_ubyte1_e32 v163, v146
	v_cvt_f32_ubyte0_e32 v162, v146
	v_pk_mul_f32 v[150:151], v[150:151], v[162:163]
	v_pk_mul_f32 v[154:155], v[154:155], v[160:161]
	v_pk_mul_f32 v[46:47], v[46:47], v[150:151]
	v_pk_mul_f32 v[48:49], v[48:49], v[154:155]
	v_cvt_f32_ubyte3_e32 v151, v147
	v_cvt_f32_ubyte2_e32 v150, v147
	v_cvt_f32_ubyte1_e32 v155, v147
	v_cvt_f32_ubyte0_e32 v154, v147
	v_pk_mul_f32 v[146:147], v[156:157], v[154:155]
	v_pk_mul_f32 v[150:151], v[158:159], v[150:151]
	v_pk_mul_f32 v[42:43], v[42:43], v[146:147]
	v_pk_mul_f32 v[44:45], v[44:45], v[150:151]
	v_cvt_f32_ubyte0_e32 v146, v152
	v_cvt_f32_ubyte1_e32 v147, v152
	v_cvt_f32_ubyte2_e32 v150, v152
	v_cvt_f32_ubyte3_e32 v151, v152
	v_rcp_iflag_f32_e32 v146, v146
	v_rcp_iflag_f32_e32 v147, v147
	v_rcp_iflag_f32_e32 v150, v150
	v_rcp_iflag_f32_e32 v151, v151
	v_cvt_f32_ubyte0_e32 v152, v153
	v_cvt_f32_ubyte1_e32 v154, v153
	v_cvt_f32_ubyte2_e32 v155, v153
	v_cvt_f32_ubyte3_e32 v156, v153
	v_rcp_iflag_f32_e32 v152, v152
	v_rcp_iflag_f32_e32 v153, v154
	v_rcp_iflag_f32_e32 v154, v155
	v_rcp_iflag_f32_e32 v155, v156
	v_cvt_f32_ubyte3_e32 v157, v148
	v_cvt_f32_ubyte2_e32 v156, v148
	v_cvt_f32_ubyte1_e32 v159, v148
	v_cvt_f32_ubyte0_e32 v158, v148
	v_pk_mul_f32 v[146:147], v[146:147], v[158:159]
	v_pk_mul_f32 v[150:151], v[150:151], v[156:157]
	v_pk_mul_f32 v[38:39], v[38:39], v[146:147]
	v_pk_mul_f32 v[40:41], v[40:41], v[150:151]
	v_cvt_f32_ubyte3_e32 v147, v149
	v_cvt_f32_ubyte2_e32 v146, v149
	v_cvt_f32_ubyte1_e32 v151, v149
	v_cvt_f32_ubyte0_e32 v150, v149
	v_pk_mul_f32 v[148:149], v[152:153], v[150:151]
	v_pk_mul_f32 v[146:147], v[154:155], v[146:147]
	v_pk_mul_f32 v[34:35], v[34:35], v[148:149]
	v_pk_mul_f32 v[36:37], v[36:37], v[146:147]
	s_waitcnt vmcnt(2)
	v_cvt_f32_ubyte0_e32 v146, v142
	v_cvt_f32_ubyte1_e32 v147, v142
	v_cvt_f32_ubyte2_e32 v148, v142
	v_cvt_f32_ubyte3_e32 v149, v142
	v_cvt_f32_ubyte0_e32 v150, v143
	v_cvt_f32_ubyte1_e32 v151, v143
	v_cvt_f32_ubyte2_e32 v152, v143
	v_cvt_f32_ubyte3_e32 v153, v143
	v_rcp_iflag_f32_e32 v142, v146
	v_rcp_iflag_f32_e32 v143, v147
	v_rcp_iflag_f32_e32 v146, v148
	v_rcp_iflag_f32_e32 v147, v149
	v_rcp_iflag_f32_e32 v148, v150
	v_rcp_iflag_f32_e32 v149, v151
	v_rcp_iflag_f32_e32 v150, v152
	v_rcp_iflag_f32_e32 v151, v153
	v_cvt_f32_ubyte3_e32 v153, v138
	v_cvt_f32_ubyte2_e32 v152, v138
	v_cvt_f32_ubyte1_e32 v155, v138
	v_cvt_f32_ubyte0_e32 v154, v138
	v_pk_mul_f32 v[142:143], v[142:143], v[154:155]
	v_pk_mul_f32 v[146:147], v[146:147], v[152:153]
	v_pk_mul_f32 v[30:31], v[30:31], v[142:143]
	v_pk_mul_f32 v[32:33], v[32:33], v[146:147]
	v_cvt_f32_ubyte3_e32 v143, v139
	v_cvt_f32_ubyte2_e32 v142, v139
	v_cvt_f32_ubyte1_e32 v147, v139
	v_cvt_f32_ubyte0_e32 v146, v139
	v_pk_mul_f32 v[138:139], v[148:149], v[146:147]
	v_pk_mul_f32 v[142:143], v[150:151], v[142:143]
	v_pk_mul_f32 v[26:27], v[26:27], v[138:139]
	v_pk_mul_f32 v[28:29], v[28:29], v[142:143]
	v_cvt_f32_ubyte0_e32 v138, v144
	v_cvt_f32_ubyte1_e32 v139, v144
	v_cvt_f32_ubyte2_e32 v142, v144
	v_cvt_f32_ubyte3_e32 v143, v144
	v_rcp_iflag_f32_e32 v138, v138
	v_rcp_iflag_f32_e32 v139, v139
	v_rcp_iflag_f32_e32 v142, v142
	v_rcp_iflag_f32_e32 v143, v143
	v_cvt_f32_ubyte0_e32 v144, v145
	v_cvt_f32_ubyte1_e32 v146, v145
	v_cvt_f32_ubyte2_e32 v147, v145
	v_cvt_f32_ubyte3_e32 v148, v145
	v_rcp_iflag_f32_e32 v144, v144
	v_rcp_iflag_f32_e32 v145, v146
	v_rcp_iflag_f32_e32 v146, v147
	v_rcp_iflag_f32_e32 v147, v148
	v_cvt_f32_ubyte3_e32 v149, v140
	v_cvt_f32_ubyte2_e32 v148, v140
	v_cvt_f32_ubyte1_e32 v151, v140
	v_cvt_f32_ubyte0_e32 v150, v140
	v_pk_mul_f32 v[138:139], v[138:139], v[150:151]
	v_pk_mul_f32 v[142:143], v[142:143], v[148:149]
	v_pk_mul_f32 v[22:23], v[22:23], v[138:139]
	v_pk_mul_f32 v[24:25], v[24:25], v[142:143]
	v_cvt_f32_ubyte3_e32 v139, v141
	v_cvt_f32_ubyte2_e32 v138, v141
	v_cvt_f32_ubyte1_e32 v143, v141
	v_cvt_f32_ubyte0_e32 v142, v141
	v_pk_mul_f32 v[140:141], v[144:145], v[142:143]
	v_pk_mul_f32 v[138:139], v[146:147], v[138:139]
	v_pk_mul_f32 v[18:19], v[18:19], v[140:141]
	v_pk_mul_f32 v[20:21], v[20:21], v[138:139]
	s_waitcnt vmcnt(0)
	v_cvt_f32_ubyte0_e32 v138, v134
	v_cvt_f32_ubyte1_e32 v139, v134
	v_cvt_f32_ubyte2_e32 v140, v134
	v_cvt_f32_ubyte3_e32 v141, v134
	v_cvt_f32_ubyte0_e32 v142, v135
	v_cvt_f32_ubyte1_e32 v143, v135
	v_cvt_f32_ubyte2_e32 v144, v135
	v_cvt_f32_ubyte3_e32 v145, v135
	v_rcp_iflag_f32_e32 v134, v138
	v_rcp_iflag_f32_e32 v135, v139
	v_rcp_iflag_f32_e32 v138, v140
	v_rcp_iflag_f32_e32 v139, v141
	v_rcp_iflag_f32_e32 v140, v142
	v_rcp_iflag_f32_e32 v141, v143
	v_rcp_iflag_f32_e32 v142, v144
	v_rcp_iflag_f32_e32 v143, v145
	v_cvt_f32_ubyte3_e32 v145, v130
	v_cvt_f32_ubyte2_e32 v144, v130
	v_cvt_f32_ubyte1_e32 v147, v130
	v_cvt_f32_ubyte0_e32 v146, v130
	v_pk_mul_f32 v[134:135], v[134:135], v[146:147]
	v_pk_mul_f32 v[138:139], v[138:139], v[144:145]
	v_pk_mul_f32 v[14:15], v[14:15], v[134:135]
	v_pk_mul_f32 v[16:17], v[16:17], v[138:139]
	v_cvt_f32_ubyte3_e32 v135, v131
	v_cvt_f32_ubyte2_e32 v134, v131
	v_cvt_f32_ubyte1_e32 v139, v131
	v_cvt_f32_ubyte0_e32 v138, v131
	v_pk_mul_f32 v[130:131], v[140:141], v[138:139]
	v_pk_mul_f32 v[134:135], v[142:143], v[134:135]
	v_pk_mul_f32 v[10:11], v[10:11], v[130:131]
	v_pk_mul_f32 v[12:13], v[12:13], v[134:135]
	v_cvt_f32_ubyte0_e32 v130, v136
	v_cvt_f32_ubyte1_e32 v131, v136
	v_cvt_f32_ubyte2_e32 v134, v136
	v_cvt_f32_ubyte3_e32 v135, v136
	v_rcp_iflag_f32_e32 v130, v130
	v_rcp_iflag_f32_e32 v131, v131
	v_rcp_iflag_f32_e32 v134, v134
	v_rcp_iflag_f32_e32 v135, v135
	v_cvt_f32_ubyte0_e32 v136, v137
	v_cvt_f32_ubyte1_e32 v138, v137
	v_cvt_f32_ubyte2_e32 v139, v137
	v_cvt_f32_ubyte3_e32 v140, v137
	v_rcp_iflag_f32_e32 v136, v136
	v_rcp_iflag_f32_e32 v137, v138
	v_rcp_iflag_f32_e32 v138, v139
	v_rcp_iflag_f32_e32 v139, v140
	v_cvt_f32_ubyte3_e32 v141, v132
	v_cvt_f32_ubyte2_e32 v140, v132
	v_cvt_f32_ubyte1_e32 v143, v132
	v_cvt_f32_ubyte0_e32 v142, v132
	v_pk_mul_f32 v[130:131], v[130:131], v[142:143]
	v_pk_mul_f32 v[134:135], v[134:135], v[140:141]
	v_pk_mul_f32 v[6:7], v[6:7], v[130:131]
	v_pk_mul_f32 v[8:9], v[8:9], v[134:135]
	v_cvt_f32_ubyte3_e32 v131, v133
	v_cvt_f32_ubyte2_e32 v130, v133
	v_cvt_f32_ubyte1_e32 v135, v133
	v_cvt_f32_ubyte0_e32 v134, v133
	v_pk_mul_f32 v[132:133], v[136:137], v[134:135]
	v_pk_mul_f32 v[130:131], v[138:139], v[130:131]
	v_pk_mul_f32 v[2:3], v[2:3], v[132:133]
	v_pk_mul_f32 v[4:5], v[4:5], v[130:131]
